# baseline (speedup 1.0000x reference)
.Lno_anc:
	s_or_b64 exec, exec, s[8:9]
	v_mov_b32_e32 v7, 0x80
	s_waitcnt vmcnt(0)
	s_sub_u32 s26, 0x1ff, s2
	s_mul_i32 s26, s26, 3
	s_lshr_b32 s26, s26, 5
	s_cmp_eq_u32 s26, 0
	s_cbranch_scc1 .Lhold_done
.Lhold:
	s_sleep 1
	s_sub_u32 s26, s26, 1
	s_cmp_lg_u32 s26, 0
	s_cbranch_scc1 .Lhold
.Lhold_done:
	v_cmp_ne_u32_e64 s[4:5], 0, v12
	s_nop 1
	v_cndmask_b32_e64 v8, 0, 1, s[4:5]
	v_cmp_eq_u32_e64 s[4:5], 0, v13
	s_nop 1
	v_cndmask_b32_e64 v9, 2, 0, s[4:5]
	v_cmp_eq_u32_e64 s[4:5], 0, v14
	v_or_b32_e32 v8, v9, v8
	s_nop 0
	v_cndmask_b32_e64 v12, 4, 0, s[4:5]
	v_cmp_eq_u32_e64 s[4:5], 0, v15
	s_nop 1
	v_cndmask_b32_e64 v13, 8, 0, s[4:5]
	v_cmp_eq_u32_e64 s[4:5], 0, v16
	v_or3_b32 v8, v8, v12, v13
	s_nop 0
	v_cndmask_b32_e64 v14, 16, 0, s[4:5]
	v_cmp_eq_u32_e64 s[4:5], 0, v17
	s_nop 1
	v_cndmask_b32_e64 v15, 32, 0, s[4:5]
	v_cmp_eq_u32_e64 s[4:5], 0, v18
	s_nop 1
	v_cndmask_b32_e64 v16, 64, 0, s[4:5]
	v_cmp_eq_u32_e64 s[4:5], 0, v19
	s_nop 1
	v_cndmask_b32_e64 v7, v7, 0, s[4:5]
	v_or_b32_e32 v7, v16, v7
	v_or3_b32 v9, v7, v15, v14
	v_or_b32_e32 v7, v9, v8
	v_bcnt_u32_b32 v8, v8, 0
	v_bcnt_u32_b32 v9, v9, 0
	v_lshl_or_b32 v9, v9, 16, v8
	v_cmp_ne_u32_e64 s[4:5], 0, v7
	s_nop 0
	v_add_u32_dpp v8, v9, v9 row_shr:1 row_mask:0xf bank_mask:0xf bound_ctrl:1
	s_nop 1
	v_add_u32_dpp v8, v8, v8 row_shr:2 row_mask:0xf bank_mask:0xf bound_ctrl:1
	s_nop 1
	v_add_u32_dpp v8, v8, v8 row_shr:4 row_mask:0xf bank_mask:0xf bound_ctrl:1
	s_nop 1
	v_add_u32_dpp v12, v8, v8 row_shr:8 row_mask:0xf bank_mask:0xf bound_ctrl:1
	s_nop 1
	v_add_u32_dpp v12, v12, v12 row_bcast:15 row_mask:0xa bank_mask:0xf
	s_nop 1
	v_add_u32_dpp v12, v12, v12 row_bcast:31 row_mask:0xc bank_mask:0xf
	s_nop 0
	v_readlane_b32 s14, v12, 63
	s_and_b32 s3, s14, 0xffff
	s_and_saveexec_b64 s[10:11], s[4:5]
	s_cbranch_execz .LBB0_5
	v_sub_u32_e32 v12, v12, v9
	v_lshlrev_b32_e32 v8, 10, v1
	v_add_u32_sdwa v9, sext(v12), s3 dst_sel:DWORD dst_unused:UNUSED_PAD src0_sel:WORD_1 src1_sel:DWORD
	v_and_b32_e32 v12, 0xffff, v12
	v_lshlrev_b32_e32 v13, 2, v10
	s_mov_b64 s[12:13], 0
	v_mov_b32_e32 v14, 0x100

	.amdhsa_kernel _Z12giou_partialPK15HIP_vector_typeIfLj4EES2_S2_PKiPS_IfLj2EE
		.amdhsa_group_segment_fixed_size 24704
		.amdhsa_private_segment_fixed_size 0
		.amdhsa_kernarg_size 40
		.amdhsa_user_sgpr_count 2
		.amdhsa_user_sgpr_dispatch_ptr 0
		.amdhsa_user_sgpr_queue_ptr 0
		.amdhsa_user_sgpr_kernarg_segment_ptr 1
		.amdhsa_user_sgpr_dispatch_id 0
		.amdhsa_user_sgpr_kernarg_preload_length 0
		.amdhsa_user_sgpr_kernarg_preload_offset 0
		.amdhsa_user_sgpr_private_segment_size 0
		.amdhsa_uses_dynamic_stack 0
		.amdhsa_enable_private_segment 0
		.amdhsa_system_sgpr_workgroup_id_x 1
		.amdhsa_system_sgpr_workgroup_id_y 0
		.amdhsa_system_sgpr_workgroup_id_z 0
		.amdhsa_system_sgpr_workgroup_info 0
		.amdhsa_system_vgpr_workitem_id 0
		.amdhsa_next_free_vgpr 24
		.amdhsa_next_free_sgpr 27
		.amdhsa_accum_offset 24
		.amdhsa_reserve_vcc 1
		.amdhsa_float_round_mode_32 0
		.amdhsa_float_round_mode_16_64 0
		.amdhsa_float_denorm_mode_32 3
		.amdhsa_float_denorm_mode_16_64 3
		.amdhsa_dx10_clamp 1
		.amdhsa_ieee_mode 1
		.amdhsa_fp16_overflow 0
		.amdhsa_tg_split 0
		.amdhsa_exception_fp_ieee_invalid_op 0
		.amdhsa_exception_fp_denorm_src 0
		.amdhsa_exception_fp_ieee_div_zero 0
		.amdhsa_exception_fp_ieee_overflow 0
		.amdhsa_exception_fp_ieee_underflow 0
		.amdhsa_exception_fp_ieee_inexact 0
		.amdhsa_exception_int_div_zero 0
	.end_amdhsa_kernel

.Lfunc_end0:
	.size	_Z12giou_partialPK15HIP_vector_typeIfLj4EES2_S2_PKiPS_IfLj2EE, .Lfunc_end0-_Z12giou_partialPK15HIP_vector_typeIfLj4EES2_S2_PKiPS_IfLj2EE
	.set _Z12giou_partialPK15HIP_vector_typeIfLj4EES2_S2_PKiPS_IfLj2EE.num_vgpr, 24
	.set _Z12giou_partialPK15HIP_vector_typeIfLj4EES2_S2_PKiPS_IfLj2EE.num_agpr, 0
	.set _Z12giou_partialPK15HIP_vector_typeIfLj4EES2_S2_PKiPS_IfLj2EE.numbered_sgpr, 27
	.set _Z12giou_partialPK15HIP_vector_typeIfLj4EES2_S2_PKiPS_IfLj2EE.num_named_barrier, 0
	.set _Z12giou_partialPK15HIP_vector_typeIfLj4EES2_S2_PKiPS_IfLj2EE.private_seg_size, 0
	.set _Z12giou_partialPK15HIP_vector_typeIfLj4EES2_S2_PKiPS_IfLj2EE.uses_vcc, 1
	.set _Z12giou_partialPK15HIP_vector_typeIfLj4EES2_S2_PKiPS_IfLj2EE.uses_flat_scratch, 0
	.set _Z12giou_partialPK15HIP_vector_typeIfLj4EES2_S2_PKiPS_IfLj2EE.has_dyn_sized_stack, 0
	.set _Z12giou_partialPK15HIP_vector_typeIfLj4EES2_S2_PKiPS_IfLj2EE.has_recursion, 0
	.set _Z12giou_partialPK15HIP_vector_typeIfLj4EES2_S2_PKiPS_IfLj2EE.has_indirect_call, 0

amdhsa.kernels:
  - .agpr_count:     0
    .args:
      - .actual_access:  read_only
        .address_space:  global
        .offset:         0
        .size:           8
        .value_kind:     global_buffer
      - .actual_access:  read_only
        .address_space:  global
        .offset:         8
        .size:           8
        .value_kind:     global_buffer
      - .actual_access:  read_only
        .address_space:  global
        .offset:         16
        .size:           8
        .value_kind:     global_buffer
      - .actual_access:  read_only
        .address_space:  global
        .offset:         24
        .size:           8
        .value_kind:     global_buffer
      - .actual_access:  write_only
        .address_space:  global
        .offset:         32
        .size:           8
        .value_kind:     global_buffer
    .group_segment_fixed_size: 24704
    .kernarg_segment_align: 8
    .kernarg_segment_size: 40
    .language:       OpenCL C
    .language_version:
      - 2
      - 0
    .max_flat_workgroup_size: 1024
    .name:           _Z12giou_partialPK15HIP_vector_typeIfLj4EES2_S2_PKiPS_IfLj2EE
    .private_segment_fixed_size: 0
    .sgpr_count:     33
    .sgpr_spill_count: 0
    .symbol:         _Z12giou_partialPK15HIP_vector_typeIfLj4EES2_S2_PKiPS_IfLj2EE.kd
    .uniform_work_group_size: 1
    .uses_dynamic_stack: false
    .vgpr_count:     24
    .vgpr_spill_count: 0
    .wavefront_size: 64
  - .agpr_count:     0
    .args:
      - .actual_access:  read_only
        .address_space:  global
        .offset:         0
        .size:           8
        .value_kind:     global_buffer
      - .actual_access:  write_only
        .address_space:  global
        .offset:         8
        .size:           8
        .value_kind:     global_buffer
    .group_segment_fixed_size: 0
    .kernarg_segment_align: 8
    .kernarg_segment_size: 16
    .language:       OpenCL C
    .language_version:
      - 2
      - 0
    .max_flat_workgroup_size: 64
    .name:           _Z10giou_finalPK15HIP_vector_typeIfLj2EEPf
    .private_segment_fixed_size: 0
    .sgpr_count:     18
    .sgpr_spill_count: 0
    .symbol:         _Z10giou_finalPK15HIP_vector_typeIfLj2EEPf.kd
    .uniform_work_group_size: 1
    .uses_dynamic_stack: false
    .vgpr_count:     18
    .vgpr_spill_count: 0
    .wavefront_size: 64
